# MoE-down epilogue: leading group's alignment barrier placed three quarters through its epilogue instead of at its tail
# baseline (speedup 1.0000x reference)
; __device__ __forceinline__ unsigned cvt4_fp8(float a, float b, float c, float d) { int w = 0; w = __builtin_amdgcn_cvt_pk_fp8_f32(a, b, w, false); w = __builtin_amdgcn_cvt_pk_fp8_f32(c, d, w, true); return (unsigned)w; }
; template <class Epi, class Sched, bool GATHER, bool ALIGN_EPI, bool SP2, bool FP8>
; __device__ __forceinline__ void gemm_phase(LAS unsigned char* lds, const Gemm g, const Sched& S, const Epi& E) {
;     ...
;             asm volatile("s_nop 15\n\ts_nop 3" : "+v"(acc[0][0][0][0]), "+v"(acc[0][0][0][1]), "+v"(acc[0][0][1][0]), "+v"(acc[0][0][1][1]), "+v"(acc[0][0][2][0]), "+v"(acc[0][0][2][1]), "+v"(acc[0][0][3][0]), "+v"(acc[0][0][3][1]));
;     __device__ __forceinline__ void operator()(const f32x4 (&acc)[2][2][4][2], const pg8::Unit& u, const Pre& pre, int wr, int wc, int fr, int fq) const {
;         const int e = u.e, cn = u.pn - e * 8, col0 = cn * 256 + wc * 32 + 8 * fq;
;         f32x4 bv[2][2];
; #pragma unroll
;         for (int bj = 0; bj < 2; ++bj) { bv[bj][0] = pre.bv[bj][0]; bv[bj][1] = pre.bv[bj][1]; }
; #pragma unroll
;         for (int ai = 0; ai < 2; ++ai)
; #pragma unroll
;             for (int m = 0; m < 4; ++m) { unsigned char* rowp = YS + (size_t)(u.pm * 256 + ai * 128 + wr * 64 + m * 16 + fr) * DM + col0;
; #pragma unroll
;                 for (int bj = 0; bj < 2; ++bj) { const f32x4 v0 = acc[ai][bj][m][0] * 0.015625f + bv[bj][0], v1 = acc[ai][bj][m][1] * 0.015625f + bv[bj][1];
;                     u32x2 w; w.x = cvt4_fp8(v0[0], v0[1], v0[2], v0[3]); w.y = cvt4_fp8(v1[0], v1[1], v1[2], v1[3]);
;                     *(u32x2*)(rowp + bj * 128) = w; } }
.LBB0_1008:
.LBB0_1010:
	s_nop 15
	s_nop 3
	s_waitcnt vmcnt(18)
	v_pk_fma_f32 v[8:9], v[158:159], s[18:19], v[26:27] op_sel_hi:[1,0,1]
	v_pk_fma_f32 v[10:11], v[154:155], s[18:19], v[22:23] op_sel_hi:[1,0,1]
	v_cvt_pk_fp8_f32 v12, v8, v9
	v_cvt_pk_fp8_f32 v13, v10, v11
	v_mov_b32_e32 v3, v0
	v_pk_fma_f32 v[8:9], v[160:161], s[18:19], v[28:29] op_sel_hi:[1,0,1]
	v_readfirstlane_b32 s10, v3
	v_pk_fma_f32 v[10:11], v[156:157], s[18:19], v[24:25] op_sel_hi:[1,0,1]
	s_lshr_b32 s33, s10, 1
	s_ashr_i32 s10, s10, 2
	v_cvt_pk_fp8_f32 v12, v8, v9 op_sel:[0,0,1]
	v_cvt_pk_fp8_f32 v13, v10, v11 op_sel:[0,0,1]
	s_waitcnt vmcnt(16)
	v_pk_fma_f32 v[8:9], v[150:151], s[18:19], v[30:31] op_sel_hi:[1,0,1]
	v_pk_fma_f32 v[10:11], v[146:147], s[18:19], v[18:19] op_sel_hi:[1,0,1]
	s_andn2_b32 s10, s10, 63
	v_cvt_pk_fp8_f32 v14, v8, v9
	v_cvt_pk_fp8_f32 v15, v10, v11
	s_lshl_b32 s11, s65, 8
	s_lshl_b32 s65, s66, 11
	v_and_or_b32 v4, v3, 15, s10
	s_and_b32 s33, s33, 0x60
	s_sub_i32 s11, s11, s65
	v_lshl_add_u32 v4, s62, 8, v4
	v_lshrrev_b32_e32 v2, 1, v3
	s_or_b32 s11, s33, s11
	v_ashrrev_i32_e32 v5, 31, v4
	v_pk_fma_f32 v[8:9], v[152:153], s[18:19], v[32:33] op_sel_hi:[1,0,1]
	v_pk_fma_f32 v[10:11], v[148:149], s[18:19], v[20:21] op_sel_hi:[1,0,1]
	v_and_or_b32 v2, v2, 24, s11
	v_lshlrev_b64 v[6:7], 11, v[4:5]
	v_cvt_pk_fp8_f32 v14, v8, v9 op_sel:[0,0,1]
	v_cvt_pk_fp8_f32 v15, v10, v11 op_sel:[0,0,1]
	v_ashrrev_i32_e32 v3, 31, v2
	v_lshl_add_u64 v[6:7], s[14:15], 0, v[6:7]
	v_lshl_add_u64 v[6:7], v[6:7], 0, v[2:3]
	global_store_dwordx2 v[6:7], v[12:13], off
	global_store_dwordx2 v[6:7], v[14:15], off offset:128
	v_pk_fma_f32 v[8:9], v[142:143], s[18:19], v[26:27] op_sel_hi:[1,0,1]
	v_pk_fma_f32 v[10:11], v[138:139], s[18:19], v[22:23] op_sel_hi:[1,0,1]
	v_cvt_pk_fp8_f32 v12, v8, v9
	v_cvt_pk_fp8_f32 v13, v10, v11
	v_pk_fma_f32 v[8:9], v[144:145], s[18:19], v[28:29] op_sel_hi:[1,0,1]
	v_pk_fma_f32 v[10:11], v[140:141], s[18:19], v[24:25] op_sel_hi:[1,0,1]
	v_cvt_pk_fp8_f32 v12, v8, v9 op_sel:[0,0,1]
	v_cvt_pk_fp8_f32 v13, v10, v11 op_sel:[0,0,1]
	v_pk_fma_f32 v[8:9], v[134:135], s[18:19], v[30:31] op_sel_hi:[1,0,1]
	v_pk_fma_f32 v[10:11], v[130:131], s[18:19], v[18:19] op_sel_hi:[1,0,1]
	v_cvt_pk_fp8_f32 v14, v8, v9
	v_cvt_pk_fp8_f32 v15, v10, v11
	v_or_b32_e32 v6, 16, v4
	v_ashrrev_i32_e32 v7, 31, v6
	v_pk_fma_f32 v[8:9], v[136:137], s[18:19], v[32:33] op_sel_hi:[1,0,1]
	v_pk_fma_f32 v[10:11], v[132:133], s[18:19], v[20:21] op_sel_hi:[1,0,1]
	v_lshlrev_b64 v[6:7], 11, v[6:7]
	v_cvt_pk_fp8_f32 v14, v8, v9 op_sel:[0,0,1]
	v_cvt_pk_fp8_f32 v15, v10, v11 op_sel:[0,0,1]
	v_lshl_add_u64 v[6:7], s[14:15], 0, v[6:7]
	v_lshl_add_u64 v[6:7], v[6:7], 0, v[2:3]
	global_store_dwordx2 v[6:7], v[12:13], off
	global_store_dwordx2 v[6:7], v[14:15], off offset:128
	v_pk_fma_f32 v[8:9], v[126:127], s[18:19], v[26:27] op_sel_hi:[1,0,1]
	v_pk_fma_f32 v[10:11], v[122:123], s[18:19], v[22:23] op_sel_hi:[1,0,1]
	v_cvt_pk_fp8_f32 v12, v8, v9
	v_cvt_pk_fp8_f32 v13, v10, v11
	v_pk_fma_f32 v[8:9], v[128:129], s[18:19], v[28:29] op_sel_hi:[1,0,1]
	v_pk_fma_f32 v[10:11], v[124:125], s[18:19], v[24:25] op_sel_hi:[1,0,1]
	v_cvt_pk_fp8_f32 v12, v8, v9 op_sel:[0,0,1]
	v_cvt_pk_fp8_f32 v13, v10, v11 op_sel:[0,0,1]
	v_pk_fma_f32 v[8:9], v[118:119], s[18:19], v[30:31] op_sel_hi:[1,0,1]
	v_pk_fma_f32 v[10:11], v[114:115], s[18:19], v[18:19] op_sel_hi:[1,0,1]
	v_cvt_pk_fp8_f32 v14, v8, v9
	v_cvt_pk_fp8_f32 v15, v10, v11
	v_or_b32_e32 v6, 32, v4
	v_ashrrev_i32_e32 v7, 31, v6
	v_pk_fma_f32 v[8:9], v[120:121], s[18:19], v[32:33] op_sel_hi:[1,0,1]
	v_pk_fma_f32 v[10:11], v[116:117], s[18:19], v[20:21] op_sel_hi:[1,0,1]
	v_lshlrev_b64 v[6:7], 11, v[6:7]
	v_cvt_pk_fp8_f32 v14, v8, v9 op_sel:[0,0,1]
	v_cvt_pk_fp8_f32 v15, v10, v11 op_sel:[0,0,1]
	v_lshl_add_u64 v[6:7], s[14:15], 0, v[6:7]
	v_lshl_add_u64 v[6:7], v[6:7], 0, v[2:3]
	global_store_dwordx2 v[6:7], v[12:13], off
	global_store_dwordx2 v[6:7], v[14:15], off offset:128
	v_pk_fma_f32 v[8:9], v[110:111], s[18:19], v[26:27] op_sel_hi:[1,0,1]
	v_pk_fma_f32 v[10:11], v[106:107], s[18:19], v[22:23] op_sel_hi:[1,0,1]
	v_cvt_pk_fp8_f32 v12, v8, v9
	v_cvt_pk_fp8_f32 v13, v10, v11
	v_pk_fma_f32 v[8:9], v[112:113], s[18:19], v[28:29] op_sel_hi:[1,0,1]
	v_pk_fma_f32 v[10:11], v[108:109], s[18:19], v[24:25] op_sel_hi:[1,0,1]
	v_cvt_pk_fp8_f32 v12, v8, v9 op_sel:[0,0,1]
	v_cvt_pk_fp8_f32 v13, v10, v11 op_sel:[0,0,1]
	v_pk_fma_f32 v[8:9], v[102:103], s[18:19], v[30:31] op_sel_hi:[1,0,1]
	v_pk_fma_f32 v[10:11], v[98:99], s[18:19], v[18:19] op_sel_hi:[1,0,1]
	v_cvt_pk_fp8_f32 v14, v8, v9
	v_cvt_pk_fp8_f32 v15, v10, v11
	v_or_b32_e32 v6, 48, v4
	v_ashrrev_i32_e32 v7, 31, v6
	v_pk_fma_f32 v[8:9], v[104:105], s[18:19], v[32:33] op_sel_hi:[1,0,1]
	v_pk_fma_f32 v[10:11], v[100:101], s[18:19], v[20:21] op_sel_hi:[1,0,1]
	v_lshlrev_b64 v[6:7], 11, v[6:7]
	v_cvt_pk_fp8_f32 v14, v8, v9 op_sel:[0,0,1]
	v_cvt_pk_fp8_f32 v15, v10, v11 op_sel:[0,0,1]
	v_lshl_add_u64 v[6:7], s[14:15], 0, v[6:7]
; __device__ __forceinline__ unsigned cvt4_fp8(float a, float b, float c, float d) { int w = 0; w = __builtin_amdgcn_cvt_pk_fp8_f32(a, b, w, false); w = __builtin_amdgcn_cvt_pk_fp8_f32(c, d, w, true); return (unsigned)w; }
; #define PG8_BAR __builtin_amdgcn_s_barrier()
; template <class Epi, class Sched, bool GATHER, bool ALIGN_EPI, bool SP2, bool FP8>
; __device__ __forceinline__ void gemm_phase(LAS unsigned char* lds, const Gemm g, const Sched& S, const Epi& E) {
;     ...
;         if constexpr (ALIGN_EPI) { if (wr == 0) PG8_BAR; }
;     __device__ __forceinline__ void operator()(const f32x4 (&acc)[2][2][4][2], const pg8::Unit& u, const Pre& pre, int wr, int wc, int fr, int fq) const {
;     ...
;         for (int ai = 0; ai < 2; ++ai)
; #pragma unroll
;             for (int m = 0; m < 4; ++m) { unsigned char* rowp = YS + (size_t)(u.pm * 256 + ai * 128 + wr * 64 + m * 16 + fr) * DM + col0;
; #pragma unroll
;                 for (int bj = 0; bj < 2; ++bj) { const f32x4 v0 = acc[ai][bj][m][0] * 0.015625f + bv[bj][0], v1 = acc[ai][bj][m][1] * 0.015625f + bv[bj][1];
;                     u32x2 w; w.x = cvt4_fp8(v0[0], v0[1], v0[2], v0[3]); w.y = cvt4_fp8(v1[0], v1[1], v1[2], v1[3]);
;                     *(u32x2*)(rowp + bj * 128) = w; } }
	v_lshl_add_u64 v[6:7], v[6:7], 0, v[2:3]
	global_store_dwordx2 v[6:7], v[12:13], off
	global_store_dwordx2 v[6:7], v[14:15], off offset:128
	v_pk_fma_f32 v[8:9], v[94:95], s[18:19], v[26:27] op_sel_hi:[1,0,1]
	v_pk_fma_f32 v[10:11], v[90:91], s[18:19], v[22:23] op_sel_hi:[1,0,1]
	v_cvt_pk_fp8_f32 v12, v8, v9
	v_cvt_pk_fp8_f32 v13, v10, v11
	v_pk_fma_f32 v[8:9], v[96:97], s[18:19], v[28:29] op_sel_hi:[1,0,1]
	v_pk_fma_f32 v[10:11], v[92:93], s[18:19], v[24:25] op_sel_hi:[1,0,1]
	v_cvt_pk_fp8_f32 v12, v8, v9 op_sel:[0,0,1]
	v_cvt_pk_fp8_f32 v13, v10, v11 op_sel:[0,0,1]
	v_pk_fma_f32 v[8:9], v[86:87], s[18:19], v[30:31] op_sel_hi:[1,0,1]
	v_pk_fma_f32 v[10:11], v[82:83], s[18:19], v[18:19] op_sel_hi:[1,0,1]
	v_cvt_pk_fp8_f32 v14, v8, v9
	v_cvt_pk_fp8_f32 v15, v10, v11
	v_add_u32_e32 v6, 0x80, v4
	v_ashrrev_i32_e32 v7, 31, v6
	v_pk_fma_f32 v[8:9], v[88:89], s[18:19], v[32:33] op_sel_hi:[1,0,1]
	v_pk_fma_f32 v[10:11], v[84:85], s[18:19], v[20:21] op_sel_hi:[1,0,1]
	v_lshlrev_b64 v[6:7], 11, v[6:7]
	v_cvt_pk_fp8_f32 v14, v8, v9 op_sel:[0,0,1]
	v_cvt_pk_fp8_f32 v15, v10, v11 op_sel:[0,0,1]
	v_lshl_add_u64 v[6:7], s[14:15], 0, v[6:7]
	v_lshl_add_u64 v[6:7], v[6:7], 0, v[2:3]
	global_store_dwordx2 v[6:7], v[12:13], off
	global_store_dwordx2 v[6:7], v[14:15], off offset:128
	v_pk_fma_f32 v[8:9], v[78:79], s[18:19], v[26:27] op_sel_hi:[1,0,1]
	v_pk_fma_f32 v[10:11], v[74:75], s[18:19], v[22:23] op_sel_hi:[1,0,1]
	v_cvt_pk_fp8_f32 v12, v8, v9
	v_cvt_pk_fp8_f32 v13, v10, v11
	v_pk_fma_f32 v[8:9], v[80:81], s[18:19], v[28:29] op_sel_hi:[1,0,1]
	v_pk_fma_f32 v[10:11], v[76:77], s[18:19], v[24:25] op_sel_hi:[1,0,1]
	v_cvt_pk_fp8_f32 v12, v8, v9 op_sel:[0,0,1]
	v_cvt_pk_fp8_f32 v13, v10, v11 op_sel:[0,0,1]
	v_pk_fma_f32 v[8:9], v[70:71], s[18:19], v[30:31] op_sel_hi:[1,0,1]
	v_pk_fma_f32 v[10:11], v[66:67], s[18:19], v[18:19] op_sel_hi:[1,0,1]
	v_cvt_pk_fp8_f32 v14, v8, v9
	v_cvt_pk_fp8_f32 v15, v10, v11
	v_add_u32_e32 v6, 0x90, v4
	v_ashrrev_i32_e32 v7, 31, v6
	v_pk_fma_f32 v[8:9], v[72:73], s[18:19], v[32:33] op_sel_hi:[1,0,1]
	v_pk_fma_f32 v[10:11], v[68:69], s[18:19], v[20:21] op_sel_hi:[1,0,1]
	v_lshlrev_b64 v[6:7], 11, v[6:7]
	v_cvt_pk_fp8_f32 v14, v8, v9 op_sel:[0,0,1]
	v_cvt_pk_fp8_f32 v15, v10, v11 op_sel:[0,0,1]
	v_lshl_add_u64 v[6:7], s[14:15], 0, v[6:7]
	v_lshl_add_u64 v[6:7], v[6:7], 0, v[2:3]
	global_store_dwordx2 v[6:7], v[12:13], off
	global_store_dwordx2 v[6:7], v[14:15], off offset:128
	s_and_b64 vcc, exec, s[16:17]
	s_cbranch_vccz .Lhyb_p6
	s_barrier
.Lhyb_p6:
	v_pk_fma_f32 v[8:9], v[62:63], s[18:19], v[26:27] op_sel_hi:[1,0,1]
	v_pk_fma_f32 v[10:11], v[58:59], s[18:19], v[22:23] op_sel_hi:[1,0,1]
	v_cvt_pk_fp8_f32 v12, v8, v9
	v_cvt_pk_fp8_f32 v13, v10, v11
	v_pk_fma_f32 v[8:9], v[64:65], s[18:19], v[28:29] op_sel_hi:[1,0,1]
	v_pk_fma_f32 v[10:11], v[60:61], s[18:19], v[24:25] op_sel_hi:[1,0,1]
	v_cvt_pk_fp8_f32 v12, v8, v9 op_sel:[0,0,1]
	v_cvt_pk_fp8_f32 v13, v10, v11 op_sel:[0,0,1]
	v_pk_fma_f32 v[8:9], v[54:55], s[18:19], v[30:31] op_sel_hi:[1,0,1]
	v_pk_fma_f32 v[10:11], v[50:51], s[18:19], v[18:19] op_sel_hi:[1,0,1]
	v_cvt_pk_fp8_f32 v14, v8, v9
	v_cvt_pk_fp8_f32 v15, v10, v11
	v_add_u32_e32 v6, 0xa0, v4
	v_ashrrev_i32_e32 v7, 31, v6
	v_pk_fma_f32 v[8:9], v[56:57], s[18:19], v[32:33] op_sel_hi:[1,0,1]
	v_pk_fma_f32 v[10:11], v[52:53], s[18:19], v[20:21] op_sel_hi:[1,0,1]
	v_lshlrev_b64 v[6:7], 11, v[6:7]
	v_cvt_pk_fp8_f32 v14, v8, v9 op_sel:[0,0,1]
	v_cvt_pk_fp8_f32 v15, v10, v11 op_sel:[0,0,1]
	v_lshl_add_u64 v[6:7], s[14:15], 0, v[6:7]
	v_lshl_add_u64 v[6:7], v[6:7], 0, v[2:3]
	global_store_dwordx2 v[6:7], v[12:13], off
	global_store_dwordx2 v[6:7], v[14:15], off offset:128
	v_pk_fma_f32 v[6:7], v[46:47], s[18:19], v[26:27] op_sel_hi:[1,0,1]
	v_pk_fma_f32 v[8:9], v[42:43], s[18:19], v[22:23] op_sel_hi:[1,0,1]
	v_cvt_pk_fp8_f32 v10, v6, v7
	v_cvt_pk_fp8_f32 v11, v8, v9
	v_pk_fma_f32 v[6:7], v[48:49], s[18:19], v[28:29] op_sel_hi:[1,0,1]
	v_pk_fma_f32 v[8:9], v[44:45], s[18:19], v[24:25] op_sel_hi:[1,0,1]
	v_cvt_pk_fp8_f32 v10, v6, v7 op_sel:[0,0,1]
	v_cvt_pk_fp8_f32 v11, v8, v9 op_sel:[0,0,1]
	v_pk_fma_f32 v[6:7], v[38:39], s[18:19], v[30:31] op_sel_hi:[1,0,1]
	v_pk_fma_f32 v[8:9], v[34:35], s[18:19], v[18:19] op_sel_hi:[1,0,1]
	v_cvt_pk_fp8_f32 v12, v6, v7
	v_cvt_pk_fp8_f32 v13, v8, v9
	v_add_u32_e32 v4, 0xb0, v4
	v_ashrrev_i32_e32 v5, 31, v4
	v_pk_fma_f32 v[6:7], v[40:41], s[18:19], v[32:33] op_sel_hi:[1,0,1]
	v_pk_fma_f32 v[8:9], v[36:37], s[18:19], v[20:21] op_sel_hi:[1,0,1]
	v_lshlrev_b64 v[4:5], 11, v[4:5]
	v_cvt_pk_fp8_f32 v12, v6, v7 op_sel:[0,0,1]
	v_cvt_pk_fp8_f32 v13, v8, v9 op_sel:[0,0,1]
	v_lshl_add_u64 v[4:5], s[14:15], 0, v[4:5]
	v_lshl_add_u64 v[2:3], v[4:5], 0, v[2:3]
	s_andn2_b64 vcc, exec, s[0:1]
	s_mov_b64 s[0:1], -1
	global_store_dwordx2 v[2:3], v[10:11], off
	global_store_dwordx2 v[2:3], v[12:13], off offset:128
	s_cbranch_vccnz .LBB0_1001
	s_andn2_b64 vcc, exec, s[12:13]
	s_cbranch_vccnz .LBB0_1000
	s_barrier
	s_branch .LBB0_1000
